# E30: E24 + asymmetric back-edge rotation of the NSA sel-far / win-far loops: only the priority-1 waves (tid>=256) run the next-tile chain before the barrier; the other wave group keeps the original po
# baseline (speedup 1.0000x reference)
.LBB0_697:
	v_sub_f32_e32 v0, v5, v134
	v_fmamk_f32 v5, v98, 0x3fb8aa3b, v0
	v_exp_f32_e32 v98, v5
	v_fmamk_f32 v5, v99, 0x3fb8aa3b, v0
	v_exp_f32_e32 v99, v5
	v_fmamk_f32 v5, v100, 0x3fb8aa3b, v0
	v_exp_f32_e32 v100, v5
	v_fmamk_f32 v5, v101, 0x3fb8aa3b, v0
	v_exp_f32_e32 v101, v5
	v_fmamk_f32 v94, v94, 0x3fb8aa3b, v0
	v_add_f32_e32 v5, 0, v98
	v_exp_f32_e32 v94, v94
	v_fmamk_f32 v95, v95, 0x3fb8aa3b, v0
	v_add_f32_e32 v5, v99, v5
	v_exp_f32_e32 v95, v95
	v_fmamk_f32 v96, v96, 0x3fb8aa3b, v0
	v_add_f32_e32 v5, v100, v5
	v_exp_f32_e32 v96, v96
	v_fmamk_f32 v97, v97, 0x3fb8aa3b, v0
	v_add_f32_e32 v5, v101, v5
	v_exp_f32_e32 v97, v97
	v_fmamk_f32 v90, v90, 0x3fb8aa3b, v0
	v_add_f32_e32 v5, v94, v5
	v_exp_f32_e32 v90, v90
	v_fmamk_f32 v91, v91, 0x3fb8aa3b, v0
	v_add_f32_e32 v5, v95, v5
	v_exp_f32_e32 v91, v91
	v_fmamk_f32 v92, v92, 0x3fb8aa3b, v0
	v_add_f32_e32 v5, v96, v5
	v_exp_f32_e32 v92, v92
	v_fmamk_f32 v93, v93, 0x3fb8aa3b, v0
	v_add_f32_e32 v5, v97, v5
	v_exp_f32_e32 v93, v93
	v_fmamk_f32 v86, v86, 0x3fb8aa3b, v0
	v_add_f32_e32 v5, v90, v5
	v_exp_f32_e32 v198, v86
	v_fmamk_f32 v86, v87, 0x3fb8aa3b, v0
	v_add_f32_e32 v5, v91, v5
	v_exp_f32_e32 v199, v86
	v_fmamk_f32 v86, v88, 0x3fb8aa3b, v0
	v_add_f32_e32 v5, v92, v5
	v_exp_f32_e32 v200, v86
	v_fmac_f32_e32 v0, 0x3fb8aa3b, v89
	v_add_f32_e32 v5, v93, v5
	v_exp_f32_e32 v0, v0
	v_add_f32_e32 v5, v198, v5
	v_add_f32_e32 v5, v199, v5
	v_add_f32_e32 v5, v200, v5
	v_add_f32_e32 v5, v0, v5
	v_fmac_f32_e32 v5, v136, v4
	v_sub_f32_e32 v4, v137, v125
	v_fmamk_f32 v82, v82, 0x3fb8aa3b, v4
	v_exp_f32_e32 v82, v82
	v_fmamk_f32 v83, v83, 0x3fb8aa3b, v4
	v_exp_f32_e32 v83, v83
	v_fmamk_f32 v84, v84, 0x3fb8aa3b, v4
	v_exp_f32_e32 v84, v84
	v_fmamk_f32 v85, v85, 0x3fb8aa3b, v4
	v_exp_f32_e32 v85, v85
	v_fmamk_f32 v78, v78, 0x3fb8aa3b, v4
	v_add_f32_e32 v86, 0, v82
	v_exp_f32_e32 v87, v78
	v_fmamk_f32 v78, v79, 0x3fb8aa3b, v4
	v_add_f32_e32 v86, v83, v86
	v_exp_f32_e32 v88, v78
	v_fmamk_f32 v78, v80, 0x3fb8aa3b, v4
	v_add_f32_e32 v86, v84, v86
	v_exp_f32_e32 v89, v78
	v_fmamk_f32 v78, v81, 0x3fb8aa3b, v4
	v_add_f32_e32 v86, v85, v86
	v_exp_f32_e32 v81, v78
	v_fmamk_f32 v74, v74, 0x3fb8aa3b, v4
	v_add_f32_e32 v78, v87, v86
	v_exp_f32_e32 v136, v74
	v_fmamk_f32 v74, v75, 0x3fb8aa3b, v4
	v_add_f32_e32 v78, v88, v78
	v_exp_f32_e32 v137, v74
	v_fmamk_f32 v74, v76, 0x3fb8aa3b, v4
	v_add_f32_e32 v78, v89, v78
	v_exp_f32_e32 v201, v74
	v_fmamk_f32 v74, v77, 0x3fb8aa3b, v4
	v_add_f32_e32 v78, v81, v78
	v_exp_f32_e32 v202, v74
	v_fmamk_f32 v70, v70, 0x3fb8aa3b, v4
	v_add_f32_e32 v74, v136, v78
	v_exp_f32_e32 v203, v70
	v_fmamk_f32 v70, v71, 0x3fb8aa3b, v4
	v_add_f32_e32 v74, v137, v74
	v_exp_f32_e32 v204, v70
	v_fmamk_f32 v70, v72, 0x3fb8aa3b, v4
	v_add_f32_e32 v74, v201, v74
	v_exp_f32_e32 v205, v70
	v_fmac_f32_e32 v4, 0x3fb8aa3b, v73
	v_add_f32_e32 v74, v202, v74
	v_exp_f32_e32 v4, v4
	v_add_f32_e32 v70, v203, v74
	s_cmp_eq_u32 s83, 0
	v_add_f32_e32 v70, v204, v70
	v_add_f32_e32 v70, v205, v70
	s_cselect_b32 s0, 0x8000, s79
	v_add_f32_e32 v133, v4, v70
	s_add_i32 s0, s0, 0
	v_fmac_f32_e32 v133, v135, v2
	v_add_u32_e32 v2, s0, v142
	ds_read_b128 v[70:73], v2
	ds_read_b128 v[74:77], v2 offset:2048
	v_cvt_pk_bf16_f32 v78, v82, v83
	v_cvt_pk_bf16_f32 v79, v84, v85
	ds_read_b128 v[82:85], v2 offset:4096
	v_cvt_pk_bf16_f32 v80, v87, v88
	v_cvt_pk_bf16_f32 v81, v89, v81
	v_cvt_pk_bf16_f32 v86, v98, v99
	v_cvt_pk_bf16_f32 v87, v100, v101
	v_cvt_pk_bf16_f32 v88, v94, v95
	v_cvt_pk_bf16_f32 v89, v96, v97
	s_waitcnt lgkmcnt(2)
	v_mfma_f32_16x16x32_bf16 v[66:69], v[70:73], v[78:81], v[66:69]
	v_mfma_f32_16x16x32_bf16 v[34:37], v[70:73], v[86:89], v[34:37]
	ds_read_b128 v[70:73], v2 offset:6144
	s_waitcnt lgkmcnt(2)
	v_mfma_f32_16x16x32_bf16 v[62:65], v[74:77], v[78:81], v[62:65]
	v_mfma_f32_16x16x32_bf16 v[30:33], v[74:77], v[86:89], v[30:33]
	ds_read_b128 v[74:77], v2 offset:8192
	s_waitcnt lgkmcnt(2)
	v_mfma_f32_16x16x32_bf16 v[58:61], v[82:85], v[78:81], v[58:61]
	v_mfma_f32_16x16x32_bf16 v[26:29], v[82:85], v[86:89], v[26:29]
	ds_read_b128 v[82:85], v2 offset:10240
	s_waitcnt lgkmcnt(2)
	v_mfma_f32_16x16x32_bf16 v[54:57], v[70:73], v[78:81], v[54:57]
	v_mfma_f32_16x16x32_bf16 v[22:25], v[70:73], v[86:89], v[22:25]
	ds_read_b128 v[70:73], v2 offset:12288
	s_waitcnt lgkmcnt(2)
	v_mfma_f32_16x16x32_bf16 v[50:53], v[74:77], v[78:81], v[50:53]
	v_mfma_f32_16x16x32_bf16 v[18:21], v[74:77], v[86:89], v[18:21]
	ds_read_b128 v[74:77], v2 offset:14336
	v_add_u32_e32 v2, s0, v146
	s_waitcnt lgkmcnt(2)
	v_mfma_f32_16x16x32_bf16 v[46:49], v[82:85], v[78:81], v[46:49]
	v_mfma_f32_16x16x32_bf16 v[14:17], v[82:85], v[86:89], v[14:17]
	ds_read_b128 v[82:85], v2
	s_waitcnt lgkmcnt(2)
	v_mfma_f32_16x16x32_bf16 v[42:45], v[70:73], v[78:81], v[42:45]
	v_mfma_f32_16x16x32_bf16 v[10:13], v[70:73], v[86:89], v[10:13]
	ds_read_b128 v[70:73], v2 offset:2048
	s_waitcnt lgkmcnt(2)
	v_mfma_f32_16x16x32_bf16 v[38:41], v[74:77], v[78:81], v[38:41]
	v_cvt_pk_bf16_f32 v78, v90, v91
	v_cvt_pk_bf16_f32 v79, v92, v93
	v_cvt_pk_bf16_f32 v80, v198, v199
	v_mfma_f32_16x16x32_bf16 v[6:9], v[74:77], v[86:89], v[6:9]
	ds_read_b128 v[86:89], v2 offset:4096
	v_cvt_pk_bf16_f32 v74, v136, v137
	v_cvt_pk_bf16_f32 v75, v201, v202
	v_cvt_pk_bf16_f32 v76, v203, v204
	v_cvt_pk_bf16_f32 v77, v205, v4
	v_cvt_pk_bf16_f32 v81, v200, v0
	s_nop 0
	s_waitcnt lgkmcnt(2)
	v_mfma_f32_16x16x32_bf16 v[66:69], v[82:85], v[74:77], v[66:69]
	v_mfma_f32_16x16x32_bf16 v[34:37], v[82:85], v[78:81], v[34:37]
	ds_read_b128 v[82:85], v2 offset:6144
	s_waitcnt lgkmcnt(2)
	v_mfma_f32_16x16x32_bf16 v[62:65], v[70:73], v[74:77], v[62:65]
	v_mfma_f32_16x16x32_bf16 v[30:33], v[70:73], v[78:81], v[30:33]
	ds_read_b128 v[70:73], v2 offset:8192
	s_waitcnt lgkmcnt(2)
	v_mfma_f32_16x16x32_bf16 v[58:61], v[86:89], v[74:77], v[58:61]
	v_mfma_f32_16x16x32_bf16 v[26:29], v[86:89], v[78:81], v[26:29]
	ds_read_b128 v[86:89], v2 offset:10240
	s_waitcnt lgkmcnt(2)
	v_mfma_f32_16x16x32_bf16 v[54:57], v[82:85], v[74:77], v[54:57]
	v_mfma_f32_16x16x32_bf16 v[22:25], v[82:85], v[78:81], v[22:25]
	ds_read_b128 v[82:85], v2 offset:12288
	s_waitcnt lgkmcnt(2)
	v_mfma_f32_16x16x32_bf16 v[50:53], v[70:73], v[74:77], v[50:53]
	v_mfma_f32_16x16x32_bf16 v[18:21], v[70:73], v[78:81], v[18:21]
	ds_read_b128 v[70:73], v2 offset:14336
	s_waitcnt lgkmcnt(2)
	v_mfma_f32_16x16x32_bf16 v[46:49], v[86:89], v[74:77], v[46:49]
	v_mfma_f32_16x16x32_bf16 v[14:17], v[86:89], v[78:81], v[14:17]
	s_waitcnt lgkmcnt(1)
	v_mfma_f32_16x16x32_bf16 v[42:45], v[82:85], v[74:77], v[42:45]
	v_mfma_f32_16x16x32_bf16 v[10:13], v[82:85], v[78:81], v[10:13]
	s_waitcnt lgkmcnt(0)
	v_mfma_f32_16x16x32_bf16 v[38:41], v[70:73], v[74:77], v[38:41]
	s_waitcnt vmcnt(0)
	s_add_i32 s33, s33, 1
	s_add_i32 s0, s8, s33
	v_mfma_f32_16x16x32_bf16 v[6:9], v[70:73], v[78:81], v[6:9]
	s_cmp_eq_u32 s0, 1
	s_cbranch_scc1 .Lx687_exit
	v_readfirstlane_b32 s98, v226
	s_cmpk_lt_u32 s98, 0x100
	s_cbranch_scc1 .Lx687_orig
	v_mov_b32_e32 v136, v5
	v_mov_b32_e32 v135, v133
	v_mov_b32_e32 v133, v125
	v_mov_b32_e32 v4, v134
	s_add_i32 s0, s33, -1
	s_and_b32 s83, s0, 1
	s_add_i32 s3, s3, 1
	s_lshl_b32 s0, s83, 14
	s_add_i32 s0, s0, 0
	v_add_u32_e32 v0, s0, v140
	s_add_i32 s1, s37, s33
	s_add_i32 s1, s1, -1
	s_mov_b32 s32, 0
	s_add_i32 s98, s33, -1
	s_cmp_ge_u32 s98, s86
	s_cbranch_scc1 .Lx687_pd
	s_cmp_ge_i32 s33, s42
	s_mov_b64 s[98:99], -1
	s_cbranch_scc0 .Lx687_a
	s_add_i32 s98, s8, s33
	s_cmp_ge_i32 s98, s43
	s_cselect_b32 s99, s82, 0
	s_add_i32 s22, s98, s99
	s_mov_b64 s[98:99], 0

.Lx687_orig:
	s_waitcnt vmcnt(0)
	s_barrier
	v_mov_b32_e32 v136, v5
	v_mov_b32_e32 v135, v133
	v_mov_b32_e32 v133, v125
	v_mov_b32_e32 v4, v134
	s_branch .LBB0_687

.LBB0_805:
	v_sub_f32_e32 v0, v125, v134
	v_fmamk_f32 v5, v98, 0x3fb8aa3b, v0
	v_exp_f32_e32 v98, v5
	v_fmamk_f32 v5, v99, 0x3fb8aa3b, v0
	v_exp_f32_e32 v99, v5
	v_fmamk_f32 v5, v100, 0x3fb8aa3b, v0
	v_exp_f32_e32 v100, v5
	v_fmamk_f32 v5, v101, 0x3fb8aa3b, v0
	v_exp_f32_e32 v101, v5
	v_fmamk_f32 v94, v94, 0x3fb8aa3b, v0
	v_add_f32_e32 v5, 0, v98
	v_exp_f32_e32 v94, v94
	v_fmamk_f32 v95, v95, 0x3fb8aa3b, v0
	v_add_f32_e32 v5, v99, v5
	v_exp_f32_e32 v95, v95
	v_fmamk_f32 v96, v96, 0x3fb8aa3b, v0
	v_add_f32_e32 v5, v100, v5
	v_exp_f32_e32 v96, v96
	v_fmamk_f32 v97, v97, 0x3fb8aa3b, v0
	v_add_f32_e32 v5, v101, v5
	v_exp_f32_e32 v97, v97
	v_fmamk_f32 v90, v90, 0x3fb8aa3b, v0
	v_add_f32_e32 v5, v94, v5
	v_exp_f32_e32 v90, v90
	v_fmamk_f32 v91, v91, 0x3fb8aa3b, v0
	v_add_f32_e32 v5, v95, v5
	v_exp_f32_e32 v91, v91
	v_fmamk_f32 v92, v92, 0x3fb8aa3b, v0
	v_add_f32_e32 v5, v96, v5
	v_exp_f32_e32 v92, v92
	v_fmamk_f32 v93, v93, 0x3fb8aa3b, v0
	v_add_f32_e32 v5, v97, v5
	v_exp_f32_e32 v93, v93
	v_fmamk_f32 v86, v86, 0x3fb8aa3b, v0
	v_add_f32_e32 v5, v90, v5
	v_exp_f32_e32 v137, v86
	v_fmamk_f32 v86, v87, 0x3fb8aa3b, v0
	v_add_f32_e32 v5, v91, v5
	v_exp_f32_e32 v198, v86
	v_fmamk_f32 v86, v88, 0x3fb8aa3b, v0
	v_add_f32_e32 v5, v92, v5
	v_exp_f32_e32 v199, v86
	v_fmac_f32_e32 v0, 0x3fb8aa3b, v89
	v_add_f32_e32 v5, v93, v5
	v_exp_f32_e32 v0, v0
	v_add_f32_e32 v5, v137, v5
	v_add_f32_e32 v5, v198, v5
	v_add_f32_e32 v5, v199, v5
	v_add_f32_e32 v5, v0, v5
	v_fmac_f32_e32 v5, v136, v4
	v_sub_f32_e32 v4, v125, v133
	v_fmamk_f32 v82, v82, 0x3fb8aa3b, v4
	v_exp_f32_e32 v82, v82
	v_fmamk_f32 v83, v83, 0x3fb8aa3b, v4
	v_exp_f32_e32 v83, v83
	v_fmamk_f32 v84, v84, 0x3fb8aa3b, v4
	v_exp_f32_e32 v84, v84
	v_fmamk_f32 v85, v85, 0x3fb8aa3b, v4
	v_exp_f32_e32 v85, v85
	v_fmamk_f32 v78, v78, 0x3fb8aa3b, v4
	v_add_f32_e32 v86, 0, v82
	v_exp_f32_e32 v87, v78
	v_fmamk_f32 v78, v79, 0x3fb8aa3b, v4
	v_add_f32_e32 v86, v83, v86
	v_exp_f32_e32 v88, v78
	v_fmamk_f32 v78, v80, 0x3fb8aa3b, v4
	v_add_f32_e32 v86, v84, v86
	v_exp_f32_e32 v89, v78
	v_fmamk_f32 v78, v81, 0x3fb8aa3b, v4
	v_add_f32_e32 v86, v85, v86
	v_exp_f32_e32 v81, v78
	v_fmamk_f32 v74, v74, 0x3fb8aa3b, v4
	v_add_f32_e32 v78, v87, v86
	v_exp_f32_e32 v136, v74
	v_fmamk_f32 v74, v75, 0x3fb8aa3b, v4
	v_add_f32_e32 v78, v88, v78
	v_exp_f32_e32 v200, v74
	v_fmamk_f32 v74, v76, 0x3fb8aa3b, v4
	v_add_f32_e32 v78, v89, v78
	v_exp_f32_e32 v201, v74
	v_fmamk_f32 v74, v77, 0x3fb8aa3b, v4
	v_add_f32_e32 v78, v81, v78
	v_exp_f32_e32 v202, v74
	v_fmamk_f32 v70, v70, 0x3fb8aa3b, v4
	v_add_f32_e32 v74, v136, v78
	v_exp_f32_e32 v203, v70
	v_fmamk_f32 v70, v71, 0x3fb8aa3b, v4
	v_add_f32_e32 v74, v200, v74
	v_exp_f32_e32 v204, v70
	v_fmamk_f32 v70, v72, 0x3fb8aa3b, v4
	v_add_f32_e32 v74, v201, v74
	v_exp_f32_e32 v205, v70
	v_fmac_f32_e32 v4, 0x3fb8aa3b, v73
	v_add_f32_e32 v74, v202, v74
	v_exp_f32_e32 v4, v4
	v_add_f32_e32 v70, v203, v74
	s_cmp_eq_u32 s81, 0
	v_add_f32_e32 v70, v204, v70
	v_add_f32_e32 v70, v205, v70
	s_cselect_b32 s0, 0x8000, s79
	v_add_f32_e32 v125, v4, v70
	s_add_i32 s0, s0, 0
	v_fmac_f32_e32 v125, v135, v2
	v_add_u32_e32 v2, s0, v142
	ds_read_b128 v[70:73], v2
	ds_read_b128 v[74:77], v2 offset:2048
	v_cvt_pk_bf16_f32 v78, v82, v83
	v_cvt_pk_bf16_f32 v79, v84, v85
	ds_read_b128 v[82:85], v2 offset:4096
	v_cvt_pk_bf16_f32 v80, v87, v88
	v_cvt_pk_bf16_f32 v81, v89, v81
	v_cvt_pk_bf16_f32 v86, v98, v99
	v_cvt_pk_bf16_f32 v87, v100, v101
	v_cvt_pk_bf16_f32 v88, v94, v95
	v_cvt_pk_bf16_f32 v89, v96, v97
	s_waitcnt lgkmcnt(2)
	v_mfma_f32_16x16x32_bf16 v[66:69], v[70:73], v[78:81], v[66:69]
	v_mfma_f32_16x16x32_bf16 v[34:37], v[70:73], v[86:89], v[34:37]
	ds_read_b128 v[70:73], v2 offset:6144
	s_waitcnt lgkmcnt(2)
	v_mfma_f32_16x16x32_bf16 v[62:65], v[74:77], v[78:81], v[62:65]
	v_mfma_f32_16x16x32_bf16 v[30:33], v[74:77], v[86:89], v[30:33]
	ds_read_b128 v[74:77], v2 offset:8192
	s_waitcnt lgkmcnt(2)
	v_mfma_f32_16x16x32_bf16 v[58:61], v[82:85], v[78:81], v[58:61]
	v_mfma_f32_16x16x32_bf16 v[26:29], v[82:85], v[86:89], v[26:29]
	ds_read_b128 v[82:85], v2 offset:10240
	s_waitcnt lgkmcnt(2)
	v_mfma_f32_16x16x32_bf16 v[54:57], v[70:73], v[78:81], v[54:57]
	v_mfma_f32_16x16x32_bf16 v[22:25], v[70:73], v[86:89], v[22:25]
	ds_read_b128 v[70:73], v2 offset:12288
	s_waitcnt lgkmcnt(2)
	v_mfma_f32_16x16x32_bf16 v[50:53], v[74:77], v[78:81], v[50:53]
	v_mfma_f32_16x16x32_bf16 v[18:21], v[74:77], v[86:89], v[18:21]
	ds_read_b128 v[74:77], v2 offset:14336
	v_add_u32_e32 v2, s0, v146
	s_waitcnt lgkmcnt(2)
	v_mfma_f32_16x16x32_bf16 v[46:49], v[82:85], v[78:81], v[46:49]
	v_mfma_f32_16x16x32_bf16 v[14:17], v[82:85], v[86:89], v[14:17]
	ds_read_b128 v[82:85], v2
	s_waitcnt lgkmcnt(2)
	v_mfma_f32_16x16x32_bf16 v[42:45], v[70:73], v[78:81], v[42:45]
	v_mfma_f32_16x16x32_bf16 v[10:13], v[70:73], v[86:89], v[10:13]
	ds_read_b128 v[70:73], v2 offset:2048
	s_waitcnt lgkmcnt(2)
	v_mfma_f32_16x16x32_bf16 v[38:41], v[74:77], v[78:81], v[38:41]
	v_cvt_pk_bf16_f32 v78, v90, v91
	v_cvt_pk_bf16_f32 v79, v92, v93
	v_cvt_pk_bf16_f32 v80, v137, v198
	v_mfma_f32_16x16x32_bf16 v[6:9], v[74:77], v[86:89], v[6:9]
	ds_read_b128 v[86:89], v2 offset:4096
	v_cvt_pk_bf16_f32 v74, v136, v200
	v_cvt_pk_bf16_f32 v75, v201, v202
	v_cvt_pk_bf16_f32 v76, v203, v204
	v_cvt_pk_bf16_f32 v77, v205, v4
	v_cvt_pk_bf16_f32 v81, v199, v0
	s_nop 0
	s_waitcnt lgkmcnt(2)
	v_mfma_f32_16x16x32_bf16 v[66:69], v[82:85], v[74:77], v[66:69]
	v_mfma_f32_16x16x32_bf16 v[34:37], v[82:85], v[78:81], v[34:37]
	ds_read_b128 v[82:85], v2 offset:6144
	s_waitcnt lgkmcnt(2)
	v_mfma_f32_16x16x32_bf16 v[62:65], v[70:73], v[74:77], v[62:65]
	v_mfma_f32_16x16x32_bf16 v[30:33], v[70:73], v[78:81], v[30:33]
	ds_read_b128 v[70:73], v2 offset:8192
	s_waitcnt lgkmcnt(2)
	v_mfma_f32_16x16x32_bf16 v[58:61], v[86:89], v[74:77], v[58:61]
	v_mfma_f32_16x16x32_bf16 v[26:29], v[86:89], v[78:81], v[26:29]
	ds_read_b128 v[86:89], v2 offset:10240
	s_waitcnt lgkmcnt(2)
	v_mfma_f32_16x16x32_bf16 v[54:57], v[82:85], v[74:77], v[54:57]
	v_mfma_f32_16x16x32_bf16 v[22:25], v[82:85], v[78:81], v[22:25]
	ds_read_b128 v[82:85], v2 offset:12288
	s_waitcnt lgkmcnt(2)
	v_mfma_f32_16x16x32_bf16 v[50:53], v[70:73], v[74:77], v[50:53]
	v_mfma_f32_16x16x32_bf16 v[18:21], v[70:73], v[78:81], v[18:21]
	ds_read_b128 v[70:73], v2 offset:14336
	s_waitcnt lgkmcnt(2)
	v_mfma_f32_16x16x32_bf16 v[46:49], v[86:89], v[74:77], v[46:49]
	v_mfma_f32_16x16x32_bf16 v[14:17], v[86:89], v[78:81], v[14:17]
	s_waitcnt lgkmcnt(1)
	v_mfma_f32_16x16x32_bf16 v[42:45], v[82:85], v[74:77], v[42:45]
	v_mfma_f32_16x16x32_bf16 v[10:13], v[82:85], v[78:81], v[10:13]
	s_waitcnt lgkmcnt(0)
	v_mfma_f32_16x16x32_bf16 v[38:41], v[70:73], v[74:77], v[38:41]
	s_waitcnt vmcnt(0)
	s_add_i32 s0, s3, s47
	s_cmp_lg_u32 s0, 0
	v_mfma_f32_16x16x32_bf16 v[6:9], v[70:73], v[78:81], v[6:9]
	s_cbranch_scc0 .Lx791_exit
	v_readfirstlane_b32 s98, v226
	s_cmpk_lt_u32 s98, 0x100
	s_cbranch_scc1 .Lx791_orig
	s_mov_b32 s32, 0
	v_mov_b32_e32 v136, v5
	v_mov_b32_e32 v135, v125
	v_mov_b32_e32 v137, v133
	v_mov_b32_e32 v4, v134
	s_mov_b32 s22, s47
	s_and_b32 s81, s22, 1
	s_add_i32 s47, s22, 1
	s_cmp_ge_i32 s22, s93
	s_cbranch_scc1 .Lx791_pd

.Lx791_pd:
	s_lshl_b32 s0, s81, 14
	s_add_i32 s0, s0, 0
	v_add_u32_e32 v0, s0, v140
	s_waitcnt vmcnt(0)
	s_barrier
	ds_read_b128 v[70:73], v0
	ds_read_b128 v[74:77], v0 offset:4096
	ds_read_b128 v[78:81], v197
	ds_read_b128 v[82:85], v197 offset:4096
	ds_read_b128 v[86:89], v0 offset:8192
	ds_read_b128 v[94:97], v0 offset:12288
	s_cmp_eq_u32 s32, 0
	s_cbranch_scc1 .Lx791_body
	s_mov_b32 m0, s100
	s_nop 0
	global_load_lds_dwordx4 v[240:241], off
	s_add_i32 m0, s100, 0x400
	s_nop 0
	global_load_lds_dwordx4 v[242:243], off
	s_mov_b32 m0, s101
	s_nop 0
	global_load_lds_dwordx4 v[244:245], off
	s_add_i32 m0, s101, 0x400
	s_nop 0
	global_load_lds_dwordx4 v[246:247], off
	s_branch .Lx791_body
.Lx791_orig:
	s_waitcnt vmcnt(0)
	s_barrier
	s_branch .LBB0_791
.Lx791_exit:
	s_waitcnt vmcnt(0)
	s_barrier
	s_cmp_gt_i32 s37, s93
	s_cbranch_scc1 .LBB0_517
	s_branch .LBB0_808

.LBB0_808:
	s_sub_i32 s0, s33, s42
	s_sub_i32 s47, s0, s43
	s_add_i32 s23, s37, -1
	s_sub_i32 s81, 0, s42
	s_add_i32 s82, s23, 1
	s_cmp_lt_i32 s82, s42
	s_mov_b64 s[0:1], -1
	s_cbranch_scc1 .LBB0_815
	s_branch .LBB0_810
	s_nop 0
	s_nop 0
	s_nop 0
	s_nop 0
	s_nop 0
	s_nop 0
	s_nop 0
	s_nop 0
	s_nop 0
	s_nop 0
	s_nop 0
	s_nop 0
	s_nop 0
	s_nop 0
	s_nop 0
	s_nop 0
	s_nop 0
	s_nop 0
